# gemm2 mid hook rewritten by hand: gate words through three rotating buffers (two half-batches in flight) instead of eight serial steps
# baseline (speedup 1.0000x reference)
.LBB0_599:
	s_andn2_b64 vcc, exec, s[50:51]
	s_cbranch_vccnz .LBB0_601
	s_nop 15
	s_nop 15
	s_nop 15
	s_nop 15
	global_load_dwordx4 v[6:9], v[168:169], off
	global_load_dwordx4 v[10:13], v[168:169], off offset:16
	global_load_dwordx4 v[14:17], v[164:165], off
	global_load_dwordx4 v[18:21], v[164:165], off offset:16
	v_mad_i64_i32 v[156:157], s[50:51], v202, s94, v[166:167]
	s_mov_b64 s[100:101], 0x2000
	v_lshl_add_u64 v[156:157], v[156:157], 0, s[100:101]
	global_load_dwordx2 v[178:179], v[156:157], off offset:1024
	global_load_dwordx2 v[180:181], v[156:157], off offset:3072
	v_mad_i64_i32 v[160:161], s[50:51], v202, s94, v[166:167]
	s_mov_b64 s[100:101], 0x36000
	v_lshl_add_u64 v[160:161], v[160:161], 0, s[100:101]
	global_load_dwordx2 v[182:183], v[160:161], off offset:1024
	global_load_dwordx2 v[184:185], v[160:161], off offset:3072
	v_mad_i64_i32 v[156:157], s[50:51], v202, s94, v[166:167]
	s_mov_b64 s[100:101], 0x6a000
	v_lshl_add_u64 v[156:157], v[156:157], 0, s[100:101]
	global_load_dwordx2 v[186:187], v[156:157], off offset:1024
	global_load_dwordx2 v[188:189], v[156:157], off offset:3072
	v_mad_i64_i32 v[160:161], s[50:51], v202, s94, v[166:167]
	s_mov_b64 s[100:101], 0x9e000
	v_lshl_add_u64 v[160:161], v[160:161], 0, s[100:101]
	global_load_dwordx2 v[190:191], v[160:161], off offset:1024
	global_load_dwordx2 v[192:193], v[160:161], off offset:3072
	v_mad_i64_i32 v[156:157], s[50:51], v202, s94, v[166:167]
	s_mov_b64 s[100:101], 0x1a2000
	v_lshl_add_u64 v[156:157], v[156:157], 0, s[100:101]
	global_load_dwordx2 v[194:195], v[156:157], off offset:1024
	global_load_dwordx2 v[196:197], v[156:157], off offset:3072
	v_mad_i64_i32 v[160:161], s[50:51], v202, s94, v[166:167]
	s_mov_b64 s[100:101], 0x1d6000
	v_lshl_add_u64 v[160:161], v[160:161], 0, s[100:101]
	global_load_dwordx2 v[198:199], v[160:161], off offset:1024
	global_load_dwordx2 v[218:219], v[160:161], off offset:3072
	s_waitcnt vmcnt(8)
	v_cvt_pk_f32_fp8_e32 v[156:157], v178
	v_cvt_pk_f32_fp8_e32 v[158:159], v180
	v_fmamk_f32 v156, v156, 0x3d800000, v6
	v_fmamk_f32 v157, v157, 0x3d800000, v7
	v_fmamk_f32 v158, v158, 0x3d800000, v14
	v_fmamk_f32 v159, v159, 0x3d800000, v15
	v_mul_f32_e32 v156, 0xbfb8aa3b, v156
	v_mul_f32_e32 v157, 0xbfb8aa3b, v157
	v_mul_f32_e32 v158, 0xbfb8aa3b, v158
	v_mul_f32_e32 v159, 0xbfb8aa3b, v159
	v_exp_f32_e32 v156, v156
	v_exp_f32_e32 v157, v157
	v_exp_f32_e32 v158, v158
	v_exp_f32_e32 v159, v159
	v_pk_add_f32 v[156:157], v[156:157], 1.0 op_sel_hi:[1,0]
	v_pk_add_f32 v[158:159], v[158:159], 1.0 op_sel_hi:[1,0]
	v_rcp_f32_e32 v156, v156
	v_rcp_f32_e32 v157, v157
	v_pk_mul_f32 v[158:159], v[158:159], s[78:79] op_sel_hi:[1,0]
	v_pk_mul_f32 v[158:159], v[156:157], v[158:159]
	v_pk_mul_f32 v[146:147], v[146:147], v[158:159]
	v_cvt_pk_f32_fp8_sdwa v[160:161], v178 src0_sel:WORD_1
	v_cvt_pk_f32_fp8_sdwa v[162:163], v180 src0_sel:WORD_1
	v_fmamk_f32 v160, v160, 0x3d800000, v8
	v_fmamk_f32 v161, v161, 0x3d800000, v9
	v_fmamk_f32 v162, v162, 0x3d800000, v16
	v_fmamk_f32 v163, v163, 0x3d800000, v17
	v_mul_f32_e32 v160, 0xbfb8aa3b, v160
	v_mul_f32_e32 v161, 0xbfb8aa3b, v161
	v_mul_f32_e32 v162, 0xbfb8aa3b, v162
	v_mul_f32_e32 v163, 0xbfb8aa3b, v163
	v_exp_f32_e32 v160, v160
	v_exp_f32_e32 v161, v161
	v_exp_f32_e32 v162, v162
	v_exp_f32_e32 v163, v163
	v_pk_add_f32 v[160:161], v[160:161], 1.0 op_sel_hi:[1,0]
	v_pk_add_f32 v[162:163], v[162:163], 1.0 op_sel_hi:[1,0]
	v_rcp_f32_e32 v160, v160
	v_rcp_f32_e32 v161, v161
	v_pk_mul_f32 v[162:163], v[162:163], s[78:79] op_sel_hi:[1,0]
	v_pk_mul_f32 v[162:163], v[160:161], v[162:163]
	v_pk_mul_f32 v[148:149], v[148:149], v[162:163]
	v_cvt_pk_f32_fp8_e32 v[156:157], v179
	v_cvt_pk_f32_fp8_e32 v[158:159], v181
	v_fmamk_f32 v156, v156, 0x3d800000, v10
	v_fmamk_f32 v157, v157, 0x3d800000, v11
	v_fmamk_f32 v158, v158, 0x3d800000, v18
	v_fmamk_f32 v159, v159, 0x3d800000, v19
	v_mul_f32_e32 v156, 0xbfb8aa3b, v156
	v_mul_f32_e32 v157, 0xbfb8aa3b, v157
	v_mul_f32_e32 v158, 0xbfb8aa3b, v158
	v_mul_f32_e32 v159, 0xbfb8aa3b, v159
	v_exp_f32_e32 v156, v156
	v_exp_f32_e32 v157, v157
	v_exp_f32_e32 v158, v158
	v_exp_f32_e32 v159, v159
	v_pk_add_f32 v[156:157], v[156:157], 1.0 op_sel_hi:[1,0]
	v_pk_add_f32 v[158:159], v[158:159], 1.0 op_sel_hi:[1,0]
	v_rcp_f32_e32 v156, v156
	v_rcp_f32_e32 v157, v157
	v_pk_mul_f32 v[158:159], v[158:159], s[78:79] op_sel_hi:[1,0]
	v_pk_mul_f32 v[158:159], v[156:157], v[158:159]
	v_pk_mul_f32 v[142:143], v[142:143], v[158:159]
	v_cvt_pk_f32_fp8_sdwa v[160:161], v179 src0_sel:WORD_1
	v_cvt_pk_f32_fp8_sdwa v[162:163], v181 src0_sel:WORD_1
	v_fmamk_f32 v160, v160, 0x3d800000, v12
	v_fmamk_f32 v161, v161, 0x3d800000, v13
	v_fmamk_f32 v162, v162, 0x3d800000, v20
	v_fmamk_f32 v163, v163, 0x3d800000, v21
	v_mul_f32_e32 v160, 0xbfb8aa3b, v160
	v_mul_f32_e32 v161, 0xbfb8aa3b, v161
	v_mul_f32_e32 v162, 0xbfb8aa3b, v162
	v_mul_f32_e32 v163, 0xbfb8aa3b, v163
	v_exp_f32_e32 v160, v160
	v_exp_f32_e32 v161, v161
	v_exp_f32_e32 v162, v162
	v_exp_f32_e32 v163, v163
	v_pk_add_f32 v[160:161], v[160:161], 1.0 op_sel_hi:[1,0]
	v_pk_add_f32 v[162:163], v[162:163], 1.0 op_sel_hi:[1,0]
	v_rcp_f32_e32 v160, v160
	v_rcp_f32_e32 v161, v161
	v_pk_mul_f32 v[162:163], v[162:163], s[78:79] op_sel_hi:[1,0]
	v_pk_mul_f32 v[162:163], v[160:161], v[162:163]
	v_pk_mul_f32 v[144:145], v[144:145], v[162:163]
	v_cvt_pk_f32_fp8_e32 v[156:157], v182
	v_cvt_pk_f32_fp8_e32 v[158:159], v184
	v_fmamk_f32 v156, v156, 0x3d800000, v6
	v_fmamk_f32 v157, v157, 0x3d800000, v7
	v_fmamk_f32 v158, v158, 0x3d800000, v14
	v_fmamk_f32 v159, v159, 0x3d800000, v15
	v_mul_f32_e32 v156, 0xbfb8aa3b, v156
	v_mul_f32_e32 v157, 0xbfb8aa3b, v157
	v_mul_f32_e32 v158, 0xbfb8aa3b, v158
	v_mul_f32_e32 v159, 0xbfb8aa3b, v159
	v_exp_f32_e32 v156, v156
	v_exp_f32_e32 v157, v157
	v_exp_f32_e32 v158, v158
	v_exp_f32_e32 v159, v159
	v_pk_add_f32 v[156:157], v[156:157], 1.0 op_sel_hi:[1,0]
	v_pk_add_f32 v[158:159], v[158:159], 1.0 op_sel_hi:[1,0]
	v_rcp_f32_e32 v156, v156
	v_rcp_f32_e32 v157, v157
	v_pk_mul_f32 v[158:159], v[158:159], s[78:79] op_sel_hi:[1,0]
	v_pk_mul_f32 v[158:159], v[156:157], v[158:159]
	v_pk_mul_f32 v[138:139], v[138:139], v[158:159]
	v_cvt_pk_f32_fp8_sdwa v[160:161], v182 src0_sel:WORD_1
	v_cvt_pk_f32_fp8_sdwa v[162:163], v184 src0_sel:WORD_1
	v_fmamk_f32 v160, v160, 0x3d800000, v8
	v_fmamk_f32 v161, v161, 0x3d800000, v9
	v_fmamk_f32 v162, v162, 0x3d800000, v16
	v_fmamk_f32 v163, v163, 0x3d800000, v17
	v_mul_f32_e32 v160, 0xbfb8aa3b, v160
	v_mul_f32_e32 v161, 0xbfb8aa3b, v161
	v_mul_f32_e32 v162, 0xbfb8aa3b, v162
	v_mul_f32_e32 v163, 0xbfb8aa3b, v163
	v_exp_f32_e32 v160, v160
	v_exp_f32_e32 v161, v161
	v_exp_f32_e32 v162, v162
	v_exp_f32_e32 v163, v163
	v_pk_add_f32 v[160:161], v[160:161], 1.0 op_sel_hi:[1,0]
	v_pk_add_f32 v[162:163], v[162:163], 1.0 op_sel_hi:[1,0]
	v_rcp_f32_e32 v160, v160
	v_rcp_f32_e32 v161, v161
	v_pk_mul_f32 v[162:163], v[162:163], s[78:79] op_sel_hi:[1,0]
	v_pk_mul_f32 v[162:163], v[160:161], v[162:163]
	v_pk_mul_f32 v[140:141], v[140:141], v[162:163]
	v_cvt_pk_f32_fp8_e32 v[156:157], v183
	v_cvt_pk_f32_fp8_e32 v[158:159], v185
	v_fmamk_f32 v156, v156, 0x3d800000, v10
	v_fmamk_f32 v157, v157, 0x3d800000, v11
	v_fmamk_f32 v158, v158, 0x3d800000, v18
	v_fmamk_f32 v159, v159, 0x3d800000, v19
	v_mul_f32_e32 v156, 0xbfb8aa3b, v156
	v_mul_f32_e32 v157, 0xbfb8aa3b, v157
	v_mul_f32_e32 v158, 0xbfb8aa3b, v158
	v_mul_f32_e32 v159, 0xbfb8aa3b, v159
	v_exp_f32_e32 v156, v156
	v_exp_f32_e32 v157, v157
	v_exp_f32_e32 v158, v158
	v_exp_f32_e32 v159, v159
	v_pk_add_f32 v[156:157], v[156:157], 1.0 op_sel_hi:[1,0]
	v_pk_add_f32 v[158:159], v[158:159], 1.0 op_sel_hi:[1,0]
	v_rcp_f32_e32 v156, v156
	v_rcp_f32_e32 v157, v157
	v_pk_mul_f32 v[158:159], v[158:159], s[78:79] op_sel_hi:[1,0]
	v_pk_mul_f32 v[158:159], v[156:157], v[158:159]
	v_pk_mul_f32 v[134:135], v[134:135], v[158:159]
	v_cvt_pk_f32_fp8_sdwa v[160:161], v183 src0_sel:WORD_1
	v_cvt_pk_f32_fp8_sdwa v[162:163], v185 src0_sel:WORD_1
	v_fmamk_f32 v160, v160, 0x3d800000, v12
	v_fmamk_f32 v161, v161, 0x3d800000, v13
	v_fmamk_f32 v162, v162, 0x3d800000, v20
	v_fmamk_f32 v163, v163, 0x3d800000, v21
	v_mul_f32_e32 v160, 0xbfb8aa3b, v160
	v_mul_f32_e32 v161, 0xbfb8aa3b, v161
	v_mul_f32_e32 v162, 0xbfb8aa3b, v162
	v_mul_f32_e32 v163, 0xbfb8aa3b, v163
	v_exp_f32_e32 v160, v160
	v_exp_f32_e32 v161, v161
	v_exp_f32_e32 v162, v162
	v_exp_f32_e32 v163, v163
	v_pk_add_f32 v[160:161], v[160:161], 1.0 op_sel_hi:[1,0]
	v_pk_add_f32 v[162:163], v[162:163], 1.0 op_sel_hi:[1,0]
	v_rcp_f32_e32 v160, v160
	v_rcp_f32_e32 v161, v161
	v_pk_mul_f32 v[162:163], v[162:163], s[78:79] op_sel_hi:[1,0]
	v_pk_mul_f32 v[162:163], v[160:161], v[162:163]
	v_pk_mul_f32 v[136:137], v[136:137], v[162:163]
	v_mad_i64_i32 v[156:157], s[50:51], v202, s94, v[166:167]
	s_mov_b64 s[100:101], 0x20a000
	v_lshl_add_u64 v[156:157], v[156:157], 0, s[100:101]
	global_load_dwordx2 v[178:179], v[156:157], off offset:1024
	global_load_dwordx2 v[180:181], v[156:157], off offset:3072
	v_mad_i64_i32 v[160:161], s[50:51], v202, s94, v[166:167]
	s_mov_b64 s[100:101], 0x23e000
	v_lshl_add_u64 v[160:161], v[160:161], 0, s[100:101]
	global_load_dwordx2 v[182:183], v[160:161], off offset:1024
	global_load_dwordx2 v[184:185], v[160:161], off offset:3072
	s_waitcnt vmcnt(8)
	v_cvt_pk_f32_fp8_e32 v[156:157], v186
	v_cvt_pk_f32_fp8_e32 v[158:159], v188
	v_fmamk_f32 v156, v156, 0x3d800000, v6
	v_fmamk_f32 v157, v157, 0x3d800000, v7
	v_fmamk_f32 v158, v158, 0x3d800000, v14
	v_fmamk_f32 v159, v159, 0x3d800000, v15
	v_mul_f32_e32 v156, 0xbfb8aa3b, v156
	v_mul_f32_e32 v157, 0xbfb8aa3b, v157
	v_mul_f32_e32 v158, 0xbfb8aa3b, v158
	v_mul_f32_e32 v159, 0xbfb8aa3b, v159
	v_exp_f32_e32 v156, v156
	v_exp_f32_e32 v157, v157
	v_exp_f32_e32 v158, v158
	v_exp_f32_e32 v159, v159
	v_pk_add_f32 v[156:157], v[156:157], 1.0 op_sel_hi:[1,0]
	v_pk_add_f32 v[158:159], v[158:159], 1.0 op_sel_hi:[1,0]
	v_rcp_f32_e32 v156, v156
	v_rcp_f32_e32 v157, v157
	v_pk_mul_f32 v[158:159], v[158:159], s[78:79] op_sel_hi:[1,0]
	v_pk_mul_f32 v[158:159], v[156:157], v[158:159]
	v_pk_mul_f32 v[130:131], v[130:131], v[158:159]
	v_cvt_pk_f32_fp8_sdwa v[160:161], v186 src0_sel:WORD_1
	v_cvt_pk_f32_fp8_sdwa v[162:163], v188 src0_sel:WORD_1
	v_fmamk_f32 v160, v160, 0x3d800000, v8
	v_fmamk_f32 v161, v161, 0x3d800000, v9
	v_fmamk_f32 v162, v162, 0x3d800000, v16
	v_fmamk_f32 v163, v163, 0x3d800000, v17
	v_mul_f32_e32 v160, 0xbfb8aa3b, v160
	v_mul_f32_e32 v161, 0xbfb8aa3b, v161
	v_mul_f32_e32 v162, 0xbfb8aa3b, v162
	v_mul_f32_e32 v163, 0xbfb8aa3b, v163
	v_exp_f32_e32 v160, v160
	v_exp_f32_e32 v161, v161
	v_exp_f32_e32 v162, v162
	v_exp_f32_e32 v163, v163
	v_pk_add_f32 v[160:161], v[160:161], 1.0 op_sel_hi:[1,0]
	v_pk_add_f32 v[162:163], v[162:163], 1.0 op_sel_hi:[1,0]
	v_rcp_f32_e32 v160, v160
	v_rcp_f32_e32 v161, v161
	v_pk_mul_f32 v[162:163], v[162:163], s[78:79] op_sel_hi:[1,0]
	v_pk_mul_f32 v[162:163], v[160:161], v[162:163]
	v_pk_mul_f32 v[132:133], v[132:133], v[162:163]
	v_cvt_pk_f32_fp8_e32 v[156:157], v187
	v_cvt_pk_f32_fp8_e32 v[158:159], v189
	v_fmamk_f32 v156, v156, 0x3d800000, v10
	v_fmamk_f32 v157, v157, 0x3d800000, v11
	v_fmamk_f32 v158, v158, 0x3d800000, v18
	v_fmamk_f32 v159, v159, 0x3d800000, v19
	v_mul_f32_e32 v156, 0xbfb8aa3b, v156
	v_mul_f32_e32 v157, 0xbfb8aa3b, v157
	v_mul_f32_e32 v158, 0xbfb8aa3b, v158
	v_mul_f32_e32 v159, 0xbfb8aa3b, v159
	v_exp_f32_e32 v156, v156
	v_exp_f32_e32 v157, v157
	v_exp_f32_e32 v158, v158
	v_exp_f32_e32 v159, v159
	v_pk_add_f32 v[156:157], v[156:157], 1.0 op_sel_hi:[1,0]
	v_pk_add_f32 v[158:159], v[158:159], 1.0 op_sel_hi:[1,0]
	v_rcp_f32_e32 v156, v156
	v_rcp_f32_e32 v157, v157
	v_pk_mul_f32 v[158:159], v[158:159], s[78:79] op_sel_hi:[1,0]
	v_pk_mul_f32 v[158:159], v[156:157], v[158:159]
	v_pk_mul_f32 v[126:127], v[126:127], v[158:159]
	v_cvt_pk_f32_fp8_sdwa v[160:161], v187 src0_sel:WORD_1
	v_cvt_pk_f32_fp8_sdwa v[162:163], v189 src0_sel:WORD_1
	v_fmamk_f32 v160, v160, 0x3d800000, v12
	v_fmamk_f32 v161, v161, 0x3d800000, v13
	v_fmamk_f32 v162, v162, 0x3d800000, v20
	v_fmamk_f32 v163, v163, 0x3d800000, v21
	v_mul_f32_e32 v160, 0xbfb8aa3b, v160
	v_mul_f32_e32 v161, 0xbfb8aa3b, v161
	v_mul_f32_e32 v162, 0xbfb8aa3b, v162
	v_mul_f32_e32 v163, 0xbfb8aa3b, v163
	v_exp_f32_e32 v160, v160
	v_exp_f32_e32 v161, v161
	v_exp_f32_e32 v162, v162
	v_exp_f32_e32 v163, v163
	v_pk_add_f32 v[160:161], v[160:161], 1.0 op_sel_hi:[1,0]
	v_pk_add_f32 v[162:163], v[162:163], 1.0 op_sel_hi:[1,0]
	v_rcp_f32_e32 v160, v160
	v_rcp_f32_e32 v161, v161
	v_pk_mul_f32 v[162:163], v[162:163], s[78:79] op_sel_hi:[1,0]
	v_pk_mul_f32 v[162:163], v[160:161], v[162:163]
	v_pk_mul_f32 v[128:129], v[128:129], v[162:163]
	v_cvt_pk_f32_fp8_e32 v[156:157], v190
	v_cvt_pk_f32_fp8_e32 v[158:159], v192
	v_fmamk_f32 v156, v156, 0x3d800000, v6
	v_fmamk_f32 v157, v157, 0x3d800000, v7
	v_fmamk_f32 v158, v158, 0x3d800000, v14
	v_fmamk_f32 v159, v159, 0x3d800000, v15
	v_mul_f32_e32 v156, 0xbfb8aa3b, v156
	v_mul_f32_e32 v157, 0xbfb8aa3b, v157
	v_mul_f32_e32 v158, 0xbfb8aa3b, v158
	v_mul_f32_e32 v159, 0xbfb8aa3b, v159
	v_exp_f32_e32 v156, v156
	v_exp_f32_e32 v157, v157
	v_exp_f32_e32 v158, v158
	v_exp_f32_e32 v159, v159
	v_pk_add_f32 v[156:157], v[156:157], 1.0 op_sel_hi:[1,0]
	v_pk_add_f32 v[158:159], v[158:159], 1.0 op_sel_hi:[1,0]
	v_rcp_f32_e32 v156, v156
	v_rcp_f32_e32 v157, v157
	v_pk_mul_f32 v[158:159], v[158:159], s[78:79] op_sel_hi:[1,0]
	v_pk_mul_f32 v[158:159], v[156:157], v[158:159]
	v_pk_mul_f32 v[122:123], v[122:123], v[158:159]
	v_cvt_pk_f32_fp8_sdwa v[160:161], v190 src0_sel:WORD_1
	v_cvt_pk_f32_fp8_sdwa v[162:163], v192 src0_sel:WORD_1
	v_fmamk_f32 v160, v160, 0x3d800000, v8
	v_fmamk_f32 v161, v161, 0x3d800000, v9
	v_fmamk_f32 v162, v162, 0x3d800000, v16
	v_fmamk_f32 v163, v163, 0x3d800000, v17
	v_mul_f32_e32 v160, 0xbfb8aa3b, v160
	v_mul_f32_e32 v161, 0xbfb8aa3b, v161
	v_mul_f32_e32 v162, 0xbfb8aa3b, v162
	v_mul_f32_e32 v163, 0xbfb8aa3b, v163
	v_exp_f32_e32 v160, v160
	v_exp_f32_e32 v161, v161
	v_exp_f32_e32 v162, v162
	v_exp_f32_e32 v163, v163
	v_pk_add_f32 v[160:161], v[160:161], 1.0 op_sel_hi:[1,0]
	v_pk_add_f32 v[162:163], v[162:163], 1.0 op_sel_hi:[1,0]
	v_rcp_f32_e32 v160, v160
	v_rcp_f32_e32 v161, v161
	v_pk_mul_f32 v[162:163], v[162:163], s[78:79] op_sel_hi:[1,0]
	v_pk_mul_f32 v[162:163], v[160:161], v[162:163]
	v_pk_mul_f32 v[124:125], v[124:125], v[162:163]
	v_cvt_pk_f32_fp8_e32 v[156:157], v191
	v_cvt_pk_f32_fp8_e32 v[158:159], v193
	v_fmamk_f32 v156, v156, 0x3d800000, v10
	v_fmamk_f32 v157, v157, 0x3d800000, v11
	v_fmamk_f32 v158, v158, 0x3d800000, v18
	v_fmamk_f32 v159, v159, 0x3d800000, v19
	v_mul_f32_e32 v156, 0xbfb8aa3b, v156
	v_mul_f32_e32 v157, 0xbfb8aa3b, v157
	v_mul_f32_e32 v158, 0xbfb8aa3b, v158
	v_mul_f32_e32 v159, 0xbfb8aa3b, v159
	v_exp_f32_e32 v156, v156
	v_exp_f32_e32 v157, v157
	v_exp_f32_e32 v158, v158
	v_exp_f32_e32 v159, v159
	v_pk_add_f32 v[156:157], v[156:157], 1.0 op_sel_hi:[1,0]
	v_pk_add_f32 v[158:159], v[158:159], 1.0 op_sel_hi:[1,0]
	v_rcp_f32_e32 v156, v156
	v_rcp_f32_e32 v157, v157
	v_pk_mul_f32 v[158:159], v[158:159], s[78:79] op_sel_hi:[1,0]
	v_pk_mul_f32 v[158:159], v[156:157], v[158:159]
	v_pk_mul_f32 v[118:119], v[118:119], v[158:159]
	v_cvt_pk_f32_fp8_sdwa v[160:161], v191 src0_sel:WORD_1
	v_cvt_pk_f32_fp8_sdwa v[162:163], v193 src0_sel:WORD_1
	v_fmamk_f32 v160, v160, 0x3d800000, v12
	v_fmamk_f32 v161, v161, 0x3d800000, v13
	v_fmamk_f32 v162, v162, 0x3d800000, v20
	v_fmamk_f32 v163, v163, 0x3d800000, v21
	v_mul_f32_e32 v160, 0xbfb8aa3b, v160
	v_mul_f32_e32 v161, 0xbfb8aa3b, v161
	v_mul_f32_e32 v162, 0xbfb8aa3b, v162
	v_mul_f32_e32 v163, 0xbfb8aa3b, v163
	v_exp_f32_e32 v160, v160
	v_exp_f32_e32 v161, v161
	v_exp_f32_e32 v162, v162
	v_exp_f32_e32 v163, v163
	v_pk_add_f32 v[160:161], v[160:161], 1.0 op_sel_hi:[1,0]
	v_pk_add_f32 v[162:163], v[162:163], 1.0 op_sel_hi:[1,0]
	v_rcp_f32_e32 v160, v160
	v_rcp_f32_e32 v161, v161
	v_pk_mul_f32 v[162:163], v[162:163], s[78:79] op_sel_hi:[1,0]
	v_pk_mul_f32 v[162:163], v[160:161], v[162:163]
	v_pk_mul_f32 v[120:121], v[120:121], v[162:163]
	v_mad_i64_i32 v[156:157], s[50:51], v202, s94, v[166:167]
	s_mov_b64 s[100:101], 0x2080
	v_lshl_add_u64 v[156:157], v[156:157], 0, s[100:101]
	global_load_dwordx2 v[186:187], v[156:157], off offset:1024
	global_load_dwordx2 v[188:189], v[156:157], off offset:3072
	v_mad_i64_i32 v[160:161], s[50:51], v202, s94, v[166:167]
	s_mov_b64 s[100:101], 0x36080
	v_lshl_add_u64 v[160:161], v[160:161], 0, s[100:101]
	global_load_dwordx2 v[190:191], v[160:161], off offset:1024
	global_load_dwordx2 v[192:193], v[160:161], off offset:3072
	s_waitcnt vmcnt(8)
	v_cvt_pk_f32_fp8_e32 v[156:157], v194
	v_cvt_pk_f32_fp8_e32 v[158:159], v196
	v_fmamk_f32 v156, v156, 0x3d800000, v6
	v_fmamk_f32 v157, v157, 0x3d800000, v7
	v_fmamk_f32 v158, v158, 0x3d800000, v14
	v_fmamk_f32 v159, v159, 0x3d800000, v15
	v_mul_f32_e32 v156, 0xbfb8aa3b, v156
	v_mul_f32_e32 v157, 0xbfb8aa3b, v157
	v_mul_f32_e32 v158, 0xbfb8aa3b, v158
	v_mul_f32_e32 v159, 0xbfb8aa3b, v159
	v_exp_f32_e32 v156, v156
	v_exp_f32_e32 v157, v157
	v_exp_f32_e32 v158, v158
	v_exp_f32_e32 v159, v159
	v_pk_add_f32 v[156:157], v[156:157], 1.0 op_sel_hi:[1,0]
	v_pk_add_f32 v[158:159], v[158:159], 1.0 op_sel_hi:[1,0]
	v_rcp_f32_e32 v156, v156
	v_rcp_f32_e32 v157, v157
	v_pk_mul_f32 v[158:159], v[158:159], s[78:79] op_sel_hi:[1,0]
	v_pk_mul_f32 v[158:159], v[156:157], v[158:159]
	v_pk_mul_f32 v[114:115], v[114:115], v[158:159]
	v_cvt_pk_f32_fp8_sdwa v[160:161], v194 src0_sel:WORD_1
	v_cvt_pk_f32_fp8_sdwa v[162:163], v196 src0_sel:WORD_1
	v_fmamk_f32 v160, v160, 0x3d800000, v8
	v_fmamk_f32 v161, v161, 0x3d800000, v9
	v_fmamk_f32 v162, v162, 0x3d800000, v16
	v_fmamk_f32 v163, v163, 0x3d800000, v17
	v_mul_f32_e32 v160, 0xbfb8aa3b, v160
	v_mul_f32_e32 v161, 0xbfb8aa3b, v161
	v_mul_f32_e32 v162, 0xbfb8aa3b, v162
	v_mul_f32_e32 v163, 0xbfb8aa3b, v163
	v_exp_f32_e32 v160, v160
	v_exp_f32_e32 v161, v161
	v_exp_f32_e32 v162, v162
	v_exp_f32_e32 v163, v163
	v_pk_add_f32 v[160:161], v[160:161], 1.0 op_sel_hi:[1,0]
	v_pk_add_f32 v[162:163], v[162:163], 1.0 op_sel_hi:[1,0]
	v_rcp_f32_e32 v160, v160
	v_rcp_f32_e32 v161, v161
	v_pk_mul_f32 v[162:163], v[162:163], s[78:79] op_sel_hi:[1,0]
	v_pk_mul_f32 v[162:163], v[160:161], v[162:163]
	v_pk_mul_f32 v[116:117], v[116:117], v[162:163]
	v_cvt_pk_f32_fp8_e32 v[156:157], v195
	v_cvt_pk_f32_fp8_e32 v[158:159], v197
	v_fmamk_f32 v156, v156, 0x3d800000, v10
	v_fmamk_f32 v157, v157, 0x3d800000, v11
	v_fmamk_f32 v158, v158, 0x3d800000, v18
	v_fmamk_f32 v159, v159, 0x3d800000, v19
	v_mul_f32_e32 v156, 0xbfb8aa3b, v156
	v_mul_f32_e32 v157, 0xbfb8aa3b, v157
	v_mul_f32_e32 v158, 0xbfb8aa3b, v158
	v_mul_f32_e32 v159, 0xbfb8aa3b, v159
	v_exp_f32_e32 v156, v156
	v_exp_f32_e32 v157, v157
	v_exp_f32_e32 v158, v158
	v_exp_f32_e32 v159, v159
	v_pk_add_f32 v[156:157], v[156:157], 1.0 op_sel_hi:[1,0]
	v_pk_add_f32 v[158:159], v[158:159], 1.0 op_sel_hi:[1,0]
	v_rcp_f32_e32 v156, v156
	v_rcp_f32_e32 v157, v157
	v_pk_mul_f32 v[158:159], v[158:159], s[78:79] op_sel_hi:[1,0]
	v_pk_mul_f32 v[158:159], v[156:157], v[158:159]
	v_pk_mul_f32 v[110:111], v[110:111], v[158:159]
	v_cvt_pk_f32_fp8_sdwa v[160:161], v195 src0_sel:WORD_1
	v_cvt_pk_f32_fp8_sdwa v[162:163], v197 src0_sel:WORD_1
	v_fmamk_f32 v160, v160, 0x3d800000, v12
	v_fmamk_f32 v161, v161, 0x3d800000, v13
	v_fmamk_f32 v162, v162, 0x3d800000, v20
	v_fmamk_f32 v163, v163, 0x3d800000, v21
	v_mul_f32_e32 v160, 0xbfb8aa3b, v160
	v_mul_f32_e32 v161, 0xbfb8aa3b, v161
	v_mul_f32_e32 v162, 0xbfb8aa3b, v162
	v_mul_f32_e32 v163, 0xbfb8aa3b, v163
	v_exp_f32_e32 v160, v160
	v_exp_f32_e32 v161, v161
	v_exp_f32_e32 v162, v162
	v_exp_f32_e32 v163, v163
	v_pk_add_f32 v[160:161], v[160:161], 1.0 op_sel_hi:[1,0]
	v_pk_add_f32 v[162:163], v[162:163], 1.0 op_sel_hi:[1,0]
	v_rcp_f32_e32 v160, v160
	v_rcp_f32_e32 v161, v161
	v_pk_mul_f32 v[162:163], v[162:163], s[78:79] op_sel_hi:[1,0]
	v_pk_mul_f32 v[162:163], v[160:161], v[162:163]
	v_pk_mul_f32 v[112:113], v[112:113], v[162:163]
	v_cvt_pk_f32_fp8_e32 v[156:157], v198
	v_cvt_pk_f32_fp8_e32 v[158:159], v218
	v_fmamk_f32 v156, v156, 0x3d800000, v6
	v_fmamk_f32 v157, v157, 0x3d800000, v7
	v_fmamk_f32 v158, v158, 0x3d800000, v14
	v_fmamk_f32 v159, v159, 0x3d800000, v15
	v_mul_f32_e32 v156, 0xbfb8aa3b, v156
	v_mul_f32_e32 v157, 0xbfb8aa3b, v157
	v_mul_f32_e32 v158, 0xbfb8aa3b, v158
	v_mul_f32_e32 v159, 0xbfb8aa3b, v159
	v_exp_f32_e32 v156, v156
	v_exp_f32_e32 v157, v157
	v_exp_f32_e32 v158, v158
	v_exp_f32_e32 v159, v159
	v_pk_add_f32 v[156:157], v[156:157], 1.0 op_sel_hi:[1,0]
	v_pk_add_f32 v[158:159], v[158:159], 1.0 op_sel_hi:[1,0]
	v_rcp_f32_e32 v156, v156
	v_rcp_f32_e32 v157, v157
	v_pk_mul_f32 v[158:159], v[158:159], s[78:79] op_sel_hi:[1,0]
	v_pk_mul_f32 v[158:159], v[156:157], v[158:159]
	v_pk_mul_f32 v[106:107], v[106:107], v[158:159]
	v_cvt_pk_f32_fp8_sdwa v[160:161], v198 src0_sel:WORD_1
	v_cvt_pk_f32_fp8_sdwa v[162:163], v218 src0_sel:WORD_1
	v_fmamk_f32 v160, v160, 0x3d800000, v8
	v_fmamk_f32 v161, v161, 0x3d800000, v9
	v_fmamk_f32 v162, v162, 0x3d800000, v16
	v_fmamk_f32 v163, v163, 0x3d800000, v17
	v_mul_f32_e32 v160, 0xbfb8aa3b, v160
	v_mul_f32_e32 v161, 0xbfb8aa3b, v161
	v_mul_f32_e32 v162, 0xbfb8aa3b, v162
	v_mul_f32_e32 v163, 0xbfb8aa3b, v163
	v_exp_f32_e32 v160, v160
	v_exp_f32_e32 v161, v161
	v_exp_f32_e32 v162, v162
	v_exp_f32_e32 v163, v163
	v_pk_add_f32 v[160:161], v[160:161], 1.0 op_sel_hi:[1,0]
	v_pk_add_f32 v[162:163], v[162:163], 1.0 op_sel_hi:[1,0]
	v_rcp_f32_e32 v160, v160
	v_rcp_f32_e32 v161, v161
	v_pk_mul_f32 v[162:163], v[162:163], s[78:79] op_sel_hi:[1,0]
	v_pk_mul_f32 v[162:163], v[160:161], v[162:163]
	v_pk_mul_f32 v[108:109], v[108:109], v[162:163]
	v_cvt_pk_f32_fp8_e32 v[156:157], v199
	v_cvt_pk_f32_fp8_e32 v[158:159], v219
	v_fmamk_f32 v156, v156, 0x3d800000, v10
	v_fmamk_f32 v157, v157, 0x3d800000, v11
	v_fmamk_f32 v158, v158, 0x3d800000, v18
	v_fmamk_f32 v159, v159, 0x3d800000, v19
	v_mul_f32_e32 v156, 0xbfb8aa3b, v156
	v_mul_f32_e32 v157, 0xbfb8aa3b, v157
	v_mul_f32_e32 v158, 0xbfb8aa3b, v158
	v_mul_f32_e32 v159, 0xbfb8aa3b, v159
	v_exp_f32_e32 v156, v156
	v_exp_f32_e32 v157, v157
	v_exp_f32_e32 v158, v158
	v_exp_f32_e32 v159, v159
	v_pk_add_f32 v[156:157], v[156:157], 1.0 op_sel_hi:[1,0]
	v_pk_add_f32 v[158:159], v[158:159], 1.0 op_sel_hi:[1,0]
	v_rcp_f32_e32 v156, v156
	v_rcp_f32_e32 v157, v157
	v_pk_mul_f32 v[158:159], v[158:159], s[78:79] op_sel_hi:[1,0]
	v_pk_mul_f32 v[158:159], v[156:157], v[158:159]
	v_pk_mul_f32 v[102:103], v[102:103], v[158:159]
	v_cvt_pk_f32_fp8_sdwa v[160:161], v199 src0_sel:WORD_1
	v_cvt_pk_f32_fp8_sdwa v[162:163], v219 src0_sel:WORD_1
	v_fmamk_f32 v160, v160, 0x3d800000, v12
	v_fmamk_f32 v161, v161, 0x3d800000, v13
	v_fmamk_f32 v162, v162, 0x3d800000, v20
	v_fmamk_f32 v163, v163, 0x3d800000, v21
	v_mul_f32_e32 v160, 0xbfb8aa3b, v160
	v_mul_f32_e32 v161, 0xbfb8aa3b, v161
	v_mul_f32_e32 v162, 0xbfb8aa3b, v162
	v_mul_f32_e32 v163, 0xbfb8aa3b, v163
	v_exp_f32_e32 v160, v160
	v_exp_f32_e32 v161, v161
	v_exp_f32_e32 v162, v162
	v_exp_f32_e32 v163, v163
	v_pk_add_f32 v[160:161], v[160:161], 1.0 op_sel_hi:[1,0]
	v_pk_add_f32 v[162:163], v[162:163], 1.0 op_sel_hi:[1,0]
	v_rcp_f32_e32 v160, v160
	v_rcp_f32_e32 v161, v161
	v_pk_mul_f32 v[162:163], v[162:163], s[78:79] op_sel_hi:[1,0]
	v_pk_mul_f32 v[162:163], v[160:161], v[162:163]
	v_pk_mul_f32 v[104:105], v[104:105], v[162:163]
	v_mad_i64_i32 v[156:157], s[50:51], v202, s94, v[166:167]
	s_mov_b64 s[100:101], 0x6a080
	v_lshl_add_u64 v[156:157], v[156:157], 0, s[100:101]
	global_load_dwordx2 v[194:195], v[156:157], off offset:1024
	global_load_dwordx2 v[196:197], v[156:157], off offset:3072
	v_mad_i64_i32 v[160:161], s[50:51], v202, s94, v[166:167]
	s_mov_b64 s[100:101], 0x9e080
	v_lshl_add_u64 v[160:161], v[160:161], 0, s[100:101]
	global_load_dwordx2 v[198:199], v[160:161], off offset:1024
	global_load_dwordx2 v[218:219], v[160:161], off offset:3072
	s_waitcnt vmcnt(8)
	v_cvt_pk_f32_fp8_e32 v[156:157], v178
	v_cvt_pk_f32_fp8_e32 v[158:159], v180
	v_fmamk_f32 v156, v156, 0x3d800000, v6
	v_fmamk_f32 v157, v157, 0x3d800000, v7
	v_fmamk_f32 v158, v158, 0x3d800000, v14
	v_fmamk_f32 v159, v159, 0x3d800000, v15
	v_mul_f32_e32 v156, 0xbfb8aa3b, v156
	v_mul_f32_e32 v157, 0xbfb8aa3b, v157
	v_mul_f32_e32 v158, 0xbfb8aa3b, v158
	v_mul_f32_e32 v159, 0xbfb8aa3b, v159
	v_exp_f32_e32 v156, v156
	v_exp_f32_e32 v157, v157
	v_exp_f32_e32 v158, v158
	v_exp_f32_e32 v159, v159
	v_pk_add_f32 v[156:157], v[156:157], 1.0 op_sel_hi:[1,0]
	v_pk_add_f32 v[158:159], v[158:159], 1.0 op_sel_hi:[1,0]
	v_rcp_f32_e32 v156, v156
	v_rcp_f32_e32 v157, v157
	v_pk_mul_f32 v[158:159], v[158:159], s[78:79] op_sel_hi:[1,0]
	v_pk_mul_f32 v[158:159], v[156:157], v[158:159]
	v_pk_mul_f32 v[98:99], v[98:99], v[158:159]
	v_cvt_pk_f32_fp8_sdwa v[160:161], v178 src0_sel:WORD_1
	v_cvt_pk_f32_fp8_sdwa v[162:163], v180 src0_sel:WORD_1
	v_fmamk_f32 v160, v160, 0x3d800000, v8
	v_fmamk_f32 v161, v161, 0x3d800000, v9
	v_fmamk_f32 v162, v162, 0x3d800000, v16
	v_fmamk_f32 v163, v163, 0x3d800000, v17
	v_mul_f32_e32 v160, 0xbfb8aa3b, v160
	v_mul_f32_e32 v161, 0xbfb8aa3b, v161
	v_mul_f32_e32 v162, 0xbfb8aa3b, v162
	v_mul_f32_e32 v163, 0xbfb8aa3b, v163
	v_exp_f32_e32 v160, v160
	v_exp_f32_e32 v161, v161
	v_exp_f32_e32 v162, v162
	v_exp_f32_e32 v163, v163
	v_pk_add_f32 v[160:161], v[160:161], 1.0 op_sel_hi:[1,0]
	v_pk_add_f32 v[162:163], v[162:163], 1.0 op_sel_hi:[1,0]
	v_rcp_f32_e32 v160, v160
	v_rcp_f32_e32 v161, v161
	v_pk_mul_f32 v[162:163], v[162:163], s[78:79] op_sel_hi:[1,0]
	v_pk_mul_f32 v[162:163], v[160:161], v[162:163]
	v_pk_mul_f32 v[100:101], v[100:101], v[162:163]
	v_cvt_pk_f32_fp8_e32 v[156:157], v179
	v_cvt_pk_f32_fp8_e32 v[158:159], v181
	v_fmamk_f32 v156, v156, 0x3d800000, v10
	v_fmamk_f32 v157, v157, 0x3d800000, v11
	v_fmamk_f32 v158, v158, 0x3d800000, v18
	v_fmamk_f32 v159, v159, 0x3d800000, v19
	v_mul_f32_e32 v156, 0xbfb8aa3b, v156
	v_mul_f32_e32 v157, 0xbfb8aa3b, v157
	v_mul_f32_e32 v158, 0xbfb8aa3b, v158
	v_mul_f32_e32 v159, 0xbfb8aa3b, v159
	v_exp_f32_e32 v156, v156
	v_exp_f32_e32 v157, v157
	v_exp_f32_e32 v158, v158
	v_exp_f32_e32 v159, v159
	v_pk_add_f32 v[156:157], v[156:157], 1.0 op_sel_hi:[1,0]
	v_pk_add_f32 v[158:159], v[158:159], 1.0 op_sel_hi:[1,0]
	v_rcp_f32_e32 v156, v156
	v_rcp_f32_e32 v157, v157
	v_pk_mul_f32 v[158:159], v[158:159], s[78:79] op_sel_hi:[1,0]
	v_pk_mul_f32 v[158:159], v[156:157], v[158:159]
	v_pk_mul_f32 v[94:95], v[94:95], v[158:159]
	v_cvt_pk_f32_fp8_sdwa v[160:161], v179 src0_sel:WORD_1
	v_cvt_pk_f32_fp8_sdwa v[162:163], v181 src0_sel:WORD_1
	v_fmamk_f32 v160, v160, 0x3d800000, v12
	v_fmamk_f32 v161, v161, 0x3d800000, v13
	v_fmamk_f32 v162, v162, 0x3d800000, v20
	v_fmamk_f32 v163, v163, 0x3d800000, v21
	v_mul_f32_e32 v160, 0xbfb8aa3b, v160
	v_mul_f32_e32 v161, 0xbfb8aa3b, v161
	v_mul_f32_e32 v162, 0xbfb8aa3b, v162
	v_mul_f32_e32 v163, 0xbfb8aa3b, v163
	v_exp_f32_e32 v160, v160
	v_exp_f32_e32 v161, v161
	v_exp_f32_e32 v162, v162
	v_exp_f32_e32 v163, v163
	v_pk_add_f32 v[160:161], v[160:161], 1.0 op_sel_hi:[1,0]
	v_pk_add_f32 v[162:163], v[162:163], 1.0 op_sel_hi:[1,0]
	v_rcp_f32_e32 v160, v160
	v_rcp_f32_e32 v161, v161
	v_pk_mul_f32 v[162:163], v[162:163], s[78:79] op_sel_hi:[1,0]
	v_pk_mul_f32 v[162:163], v[160:161], v[162:163]
	v_pk_mul_f32 v[96:97], v[96:97], v[162:163]
	v_cvt_pk_f32_fp8_e32 v[156:157], v182
	v_cvt_pk_f32_fp8_e32 v[158:159], v184
	v_fmamk_f32 v156, v156, 0x3d800000, v6
	v_fmamk_f32 v157, v157, 0x3d800000, v7
	v_fmamk_f32 v158, v158, 0x3d800000, v14
	v_fmamk_f32 v159, v159, 0x3d800000, v15
	v_mul_f32_e32 v156, 0xbfb8aa3b, v156
	v_mul_f32_e32 v157, 0xbfb8aa3b, v157
	v_mul_f32_e32 v158, 0xbfb8aa3b, v158
	v_mul_f32_e32 v159, 0xbfb8aa3b, v159
	v_exp_f32_e32 v156, v156
	v_exp_f32_e32 v157, v157
	v_exp_f32_e32 v158, v158
	v_exp_f32_e32 v159, v159
	v_pk_add_f32 v[156:157], v[156:157], 1.0 op_sel_hi:[1,0]
	v_pk_add_f32 v[158:159], v[158:159], 1.0 op_sel_hi:[1,0]
	v_rcp_f32_e32 v156, v156
	v_rcp_f32_e32 v157, v157
	v_pk_mul_f32 v[158:159], v[158:159], s[78:79] op_sel_hi:[1,0]
	v_pk_mul_f32 v[158:159], v[156:157], v[158:159]
	v_pk_mul_f32 v[90:91], v[90:91], v[158:159]
	v_cvt_pk_f32_fp8_sdwa v[160:161], v182 src0_sel:WORD_1
	v_cvt_pk_f32_fp8_sdwa v[162:163], v184 src0_sel:WORD_1
	v_fmamk_f32 v160, v160, 0x3d800000, v8
	v_fmamk_f32 v161, v161, 0x3d800000, v9
	v_fmamk_f32 v162, v162, 0x3d800000, v16
	v_fmamk_f32 v163, v163, 0x3d800000, v17
	v_mul_f32_e32 v160, 0xbfb8aa3b, v160
	v_mul_f32_e32 v161, 0xbfb8aa3b, v161
	v_mul_f32_e32 v162, 0xbfb8aa3b, v162
	v_mul_f32_e32 v163, 0xbfb8aa3b, v163
	v_exp_f32_e32 v160, v160
	v_exp_f32_e32 v161, v161
	v_exp_f32_e32 v162, v162
	v_exp_f32_e32 v163, v163
	v_pk_add_f32 v[160:161], v[160:161], 1.0 op_sel_hi:[1,0]
	v_pk_add_f32 v[162:163], v[162:163], 1.0 op_sel_hi:[1,0]
	v_rcp_f32_e32 v160, v160
	v_rcp_f32_e32 v161, v161
	v_pk_mul_f32 v[162:163], v[162:163], s[78:79] op_sel_hi:[1,0]
	v_pk_mul_f32 v[162:163], v[160:161], v[162:163]
	v_pk_mul_f32 v[92:93], v[92:93], v[162:163]
	v_cvt_pk_f32_fp8_e32 v[156:157], v183
	v_cvt_pk_f32_fp8_e32 v[158:159], v185
	v_fmamk_f32 v156, v156, 0x3d800000, v10
	v_fmamk_f32 v157, v157, 0x3d800000, v11
	v_fmamk_f32 v158, v158, 0x3d800000, v18
	v_fmamk_f32 v159, v159, 0x3d800000, v19
	v_mul_f32_e32 v156, 0xbfb8aa3b, v156
	v_mul_f32_e32 v157, 0xbfb8aa3b, v157
	v_mul_f32_e32 v158, 0xbfb8aa3b, v158
	v_mul_f32_e32 v159, 0xbfb8aa3b, v159
	v_exp_f32_e32 v156, v156
	v_exp_f32_e32 v157, v157
	v_exp_f32_e32 v158, v158
	v_exp_f32_e32 v159, v159
	v_pk_add_f32 v[156:157], v[156:157], 1.0 op_sel_hi:[1,0]
	v_pk_add_f32 v[158:159], v[158:159], 1.0 op_sel_hi:[1,0]
	v_rcp_f32_e32 v156, v156
	v_rcp_f32_e32 v157, v157
	v_pk_mul_f32 v[158:159], v[158:159], s[78:79] op_sel_hi:[1,0]
	v_pk_mul_f32 v[158:159], v[156:157], v[158:159]
	v_pk_mul_f32 v[86:87], v[86:87], v[158:159]
	v_cvt_pk_f32_fp8_sdwa v[160:161], v183 src0_sel:WORD_1
	v_cvt_pk_f32_fp8_sdwa v[162:163], v185 src0_sel:WORD_1
	v_fmamk_f32 v160, v160, 0x3d800000, v12
	v_fmamk_f32 v161, v161, 0x3d800000, v13
	v_fmamk_f32 v162, v162, 0x3d800000, v20
	v_fmamk_f32 v163, v163, 0x3d800000, v21
	v_mul_f32_e32 v160, 0xbfb8aa3b, v160
	v_mul_f32_e32 v161, 0xbfb8aa3b, v161
	v_mul_f32_e32 v162, 0xbfb8aa3b, v162
	v_mul_f32_e32 v163, 0xbfb8aa3b, v163
	v_exp_f32_e32 v160, v160
	v_exp_f32_e32 v161, v161
	v_exp_f32_e32 v162, v162
	v_exp_f32_e32 v163, v163
	v_pk_add_f32 v[160:161], v[160:161], 1.0 op_sel_hi:[1,0]
	v_pk_add_f32 v[162:163], v[162:163], 1.0 op_sel_hi:[1,0]
	v_rcp_f32_e32 v160, v160
	v_rcp_f32_e32 v161, v161
	v_pk_mul_f32 v[162:163], v[162:163], s[78:79] op_sel_hi:[1,0]
	v_pk_mul_f32 v[162:163], v[160:161], v[162:163]
	v_pk_mul_f32 v[88:89], v[88:89], v[162:163]
	global_load_dwordx4 v[6:9], v[168:169], off offset:512
	global_load_dwordx4 v[10:13], v[168:169], off offset:528
	global_load_dwordx4 v[14:17], v[164:165], off offset:512
	global_load_dwordx4 v[18:21], v[164:165], off offset:528
	v_mad_i64_i32 v[156:157], s[50:51], v202, s94, v[166:167]
	s_mov_b64 s[100:101], 0x1a2080
	v_lshl_add_u64 v[156:157], v[156:157], 0, s[100:101]
	global_load_dwordx2 v[178:179], v[156:157], off offset:1024
	global_load_dwordx2 v[180:181], v[156:157], off offset:3072
	v_mad_i64_i32 v[160:161], s[50:51], v202, s94, v[166:167]
	s_mov_b64 s[100:101], 0x1d6080
	v_lshl_add_u64 v[160:161], v[160:161], 0, s[100:101]
	global_load_dwordx2 v[182:183], v[160:161], off offset:1024
	global_load_dwordx2 v[184:185], v[160:161], off offset:3072
	s_waitcnt vmcnt(4)
	s_waitcnt vmcnt(12)
	v_cvt_pk_f32_fp8_e32 v[156:157], v186
	v_cvt_pk_f32_fp8_e32 v[158:159], v188
	v_fmamk_f32 v156, v156, 0x3d800000, v6
	v_fmamk_f32 v157, v157, 0x3d800000, v7
	v_fmamk_f32 v158, v158, 0x3d800000, v14
	v_fmamk_f32 v159, v159, 0x3d800000, v15
	v_mul_f32_e32 v156, 0xbfb8aa3b, v156
	v_mul_f32_e32 v157, 0xbfb8aa3b, v157
	v_mul_f32_e32 v158, 0xbfb8aa3b, v158
	v_mul_f32_e32 v159, 0xbfb8aa3b, v159
	v_exp_f32_e32 v156, v156
	v_exp_f32_e32 v157, v157
	v_exp_f32_e32 v158, v158
	v_exp_f32_e32 v159, v159
	v_pk_add_f32 v[156:157], v[156:157], 1.0 op_sel_hi:[1,0]
	v_pk_add_f32 v[158:159], v[158:159], 1.0 op_sel_hi:[1,0]
	v_rcp_f32_e32 v156, v156
	v_rcp_f32_e32 v157, v157
	v_pk_mul_f32 v[158:159], v[158:159], s[78:79] op_sel_hi:[1,0]
	v_pk_mul_f32 v[158:159], v[156:157], v[158:159]
	v_pk_mul_f32 v[82:83], v[82:83], v[158:159]
	v_cvt_pk_f32_fp8_sdwa v[160:161], v186 src0_sel:WORD_1
	v_cvt_pk_f32_fp8_sdwa v[162:163], v188 src0_sel:WORD_1
	v_fmamk_f32 v160, v160, 0x3d800000, v8
	v_fmamk_f32 v161, v161, 0x3d800000, v9
	v_fmamk_f32 v162, v162, 0x3d800000, v16
	v_fmamk_f32 v163, v163, 0x3d800000, v17
	v_mul_f32_e32 v160, 0xbfb8aa3b, v160
	v_mul_f32_e32 v161, 0xbfb8aa3b, v161
	v_mul_f32_e32 v162, 0xbfb8aa3b, v162
	v_mul_f32_e32 v163, 0xbfb8aa3b, v163
	v_exp_f32_e32 v160, v160
	v_exp_f32_e32 v161, v161
	v_exp_f32_e32 v162, v162
	v_exp_f32_e32 v163, v163
	v_pk_add_f32 v[160:161], v[160:161], 1.0 op_sel_hi:[1,0]
	v_pk_add_f32 v[162:163], v[162:163], 1.0 op_sel_hi:[1,0]
	v_rcp_f32_e32 v160, v160
	v_rcp_f32_e32 v161, v161
	v_pk_mul_f32 v[162:163], v[162:163], s[78:79] op_sel_hi:[1,0]
	v_pk_mul_f32 v[162:163], v[160:161], v[162:163]
	v_pk_mul_f32 v[84:85], v[84:85], v[162:163]
	v_cvt_pk_f32_fp8_e32 v[156:157], v187
	v_cvt_pk_f32_fp8_e32 v[158:159], v189
	v_fmamk_f32 v156, v156, 0x3d800000, v10
	v_fmamk_f32 v157, v157, 0x3d800000, v11
	v_fmamk_f32 v158, v158, 0x3d800000, v18
	v_fmamk_f32 v159, v159, 0x3d800000, v19
	v_mul_f32_e32 v156, 0xbfb8aa3b, v156
	v_mul_f32_e32 v157, 0xbfb8aa3b, v157
	v_mul_f32_e32 v158, 0xbfb8aa3b, v158
	v_mul_f32_e32 v159, 0xbfb8aa3b, v159
	v_exp_f32_e32 v156, v156
	v_exp_f32_e32 v157, v157
	v_exp_f32_e32 v158, v158
	v_exp_f32_e32 v159, v159
	v_pk_add_f32 v[156:157], v[156:157], 1.0 op_sel_hi:[1,0]
	v_pk_add_f32 v[158:159], v[158:159], 1.0 op_sel_hi:[1,0]
	v_rcp_f32_e32 v156, v156
	v_rcp_f32_e32 v157, v157
	v_pk_mul_f32 v[158:159], v[158:159], s[78:79] op_sel_hi:[1,0]
	v_pk_mul_f32 v[158:159], v[156:157], v[158:159]
	v_pk_mul_f32 v[78:79], v[78:79], v[158:159]
	v_cvt_pk_f32_fp8_sdwa v[160:161], v187 src0_sel:WORD_1
	v_cvt_pk_f32_fp8_sdwa v[162:163], v189 src0_sel:WORD_1
	v_fmamk_f32 v160, v160, 0x3d800000, v12
	v_fmamk_f32 v161, v161, 0x3d800000, v13
	v_fmamk_f32 v162, v162, 0x3d800000, v20
	v_fmamk_f32 v163, v163, 0x3d800000, v21
	v_mul_f32_e32 v160, 0xbfb8aa3b, v160
	v_mul_f32_e32 v161, 0xbfb8aa3b, v161
	v_mul_f32_e32 v162, 0xbfb8aa3b, v162
	v_mul_f32_e32 v163, 0xbfb8aa3b, v163
	v_exp_f32_e32 v160, v160
	v_exp_f32_e32 v161, v161
	v_exp_f32_e32 v162, v162
	v_exp_f32_e32 v163, v163
	v_pk_add_f32 v[160:161], v[160:161], 1.0 op_sel_hi:[1,0]
	v_pk_add_f32 v[162:163], v[162:163], 1.0 op_sel_hi:[1,0]
	v_rcp_f32_e32 v160, v160
	v_rcp_f32_e32 v161, v161
	v_pk_mul_f32 v[162:163], v[162:163], s[78:79] op_sel_hi:[1,0]
	v_pk_mul_f32 v[162:163], v[160:161], v[162:163]
	v_pk_mul_f32 v[80:81], v[80:81], v[162:163]
	v_cvt_pk_f32_fp8_e32 v[156:157], v190
	v_cvt_pk_f32_fp8_e32 v[158:159], v192
	v_fmamk_f32 v156, v156, 0x3d800000, v6
	v_fmamk_f32 v157, v157, 0x3d800000, v7
	v_fmamk_f32 v158, v158, 0x3d800000, v14
	v_fmamk_f32 v159, v159, 0x3d800000, v15
	v_mul_f32_e32 v156, 0xbfb8aa3b, v156
	v_mul_f32_e32 v157, 0xbfb8aa3b, v157
	v_mul_f32_e32 v158, 0xbfb8aa3b, v158
	v_mul_f32_e32 v159, 0xbfb8aa3b, v159
	v_exp_f32_e32 v156, v156
	v_exp_f32_e32 v157, v157
	v_exp_f32_e32 v158, v158
	v_exp_f32_e32 v159, v159
	v_pk_add_f32 v[156:157], v[156:157], 1.0 op_sel_hi:[1,0]
	v_pk_add_f32 v[158:159], v[158:159], 1.0 op_sel_hi:[1,0]
	v_rcp_f32_e32 v156, v156
	v_rcp_f32_e32 v157, v157
	v_pk_mul_f32 v[158:159], v[158:159], s[78:79] op_sel_hi:[1,0]
	v_pk_mul_f32 v[158:159], v[156:157], v[158:159]
	v_pk_mul_f32 v[74:75], v[74:75], v[158:159]
	v_cvt_pk_f32_fp8_sdwa v[160:161], v190 src0_sel:WORD_1
	v_cvt_pk_f32_fp8_sdwa v[162:163], v192 src0_sel:WORD_1
	v_fmamk_f32 v160, v160, 0x3d800000, v8
	v_fmamk_f32 v161, v161, 0x3d800000, v9
	v_fmamk_f32 v162, v162, 0x3d800000, v16
	v_fmamk_f32 v163, v163, 0x3d800000, v17
	v_mul_f32_e32 v160, 0xbfb8aa3b, v160
	v_mul_f32_e32 v161, 0xbfb8aa3b, v161
	v_mul_f32_e32 v162, 0xbfb8aa3b, v162
	v_mul_f32_e32 v163, 0xbfb8aa3b, v163
	v_exp_f32_e32 v160, v160
	v_exp_f32_e32 v161, v161
	v_exp_f32_e32 v162, v162
	v_exp_f32_e32 v163, v163
	v_pk_add_f32 v[160:161], v[160:161], 1.0 op_sel_hi:[1,0]
	v_pk_add_f32 v[162:163], v[162:163], 1.0 op_sel_hi:[1,0]
	v_rcp_f32_e32 v160, v160
	v_rcp_f32_e32 v161, v161
	v_pk_mul_f32 v[162:163], v[162:163], s[78:79] op_sel_hi:[1,0]
	v_pk_mul_f32 v[162:163], v[160:161], v[162:163]
	v_pk_mul_f32 v[76:77], v[76:77], v[162:163]
	v_cvt_pk_f32_fp8_e32 v[156:157], v191
	v_cvt_pk_f32_fp8_e32 v[158:159], v193
	v_fmamk_f32 v156, v156, 0x3d800000, v10
	v_fmamk_f32 v157, v157, 0x3d800000, v11
	v_fmamk_f32 v158, v158, 0x3d800000, v18
	v_fmamk_f32 v159, v159, 0x3d800000, v19
	v_mul_f32_e32 v156, 0xbfb8aa3b, v156
	v_mul_f32_e32 v157, 0xbfb8aa3b, v157
	v_mul_f32_e32 v158, 0xbfb8aa3b, v158
	v_mul_f32_e32 v159, 0xbfb8aa3b, v159
	v_exp_f32_e32 v156, v156
	v_exp_f32_e32 v157, v157
	v_exp_f32_e32 v158, v158
	v_exp_f32_e32 v159, v159
	v_pk_add_f32 v[156:157], v[156:157], 1.0 op_sel_hi:[1,0]
	v_pk_add_f32 v[158:159], v[158:159], 1.0 op_sel_hi:[1,0]
	v_rcp_f32_e32 v156, v156
	v_rcp_f32_e32 v157, v157
	v_pk_mul_f32 v[158:159], v[158:159], s[78:79] op_sel_hi:[1,0]
	v_pk_mul_f32 v[158:159], v[156:157], v[158:159]
	v_pk_mul_f32 v[70:71], v[70:71], v[158:159]
	v_cvt_pk_f32_fp8_sdwa v[160:161], v191 src0_sel:WORD_1
	v_cvt_pk_f32_fp8_sdwa v[162:163], v193 src0_sel:WORD_1
	v_fmamk_f32 v160, v160, 0x3d800000, v12
	v_fmamk_f32 v161, v161, 0x3d800000, v13
	v_fmamk_f32 v162, v162, 0x3d800000, v20
	v_fmamk_f32 v163, v163, 0x3d800000, v21
	v_mul_f32_e32 v160, 0xbfb8aa3b, v160
	v_mul_f32_e32 v161, 0xbfb8aa3b, v161
	v_mul_f32_e32 v162, 0xbfb8aa3b, v162
	v_mul_f32_e32 v163, 0xbfb8aa3b, v163
	v_exp_f32_e32 v160, v160
	v_exp_f32_e32 v161, v161
	v_exp_f32_e32 v162, v162
	v_exp_f32_e32 v163, v163
	v_pk_add_f32 v[160:161], v[160:161], 1.0 op_sel_hi:[1,0]
	v_pk_add_f32 v[162:163], v[162:163], 1.0 op_sel_hi:[1,0]
	v_rcp_f32_e32 v160, v160
	v_rcp_f32_e32 v161, v161
	v_pk_mul_f32 v[162:163], v[162:163], s[78:79] op_sel_hi:[1,0]
	v_pk_mul_f32 v[162:163], v[160:161], v[162:163]
	v_pk_mul_f32 v[72:73], v[72:73], v[162:163]
	v_mad_i64_i32 v[156:157], s[50:51], v202, s94, v[166:167]
	s_mov_b64 s[100:101], 0x20a080
	v_lshl_add_u64 v[156:157], v[156:157], 0, s[100:101]
	global_load_dwordx2 v[186:187], v[156:157], off offset:1024
	global_load_dwordx2 v[188:189], v[156:157], off offset:3072
	v_mad_i64_i32 v[160:161], s[50:51], v202, s94, v[166:167]
	s_mov_b64 s[100:101], 0x23e080
	v_lshl_add_u64 v[160:161], v[160:161], 0, s[100:101]
	global_load_dwordx2 v[190:191], v[160:161], off offset:1024
	global_load_dwordx2 v[192:193], v[160:161], off offset:3072
	s_waitcnt vmcnt(12)
	v_cvt_pk_f32_fp8_e32 v[156:157], v194
	v_cvt_pk_f32_fp8_e32 v[158:159], v196
	v_fmamk_f32 v156, v156, 0x3d800000, v6
	v_fmamk_f32 v157, v157, 0x3d800000, v7
	v_fmamk_f32 v158, v158, 0x3d800000, v14
	v_fmamk_f32 v159, v159, 0x3d800000, v15
	v_mul_f32_e32 v156, 0xbfb8aa3b, v156
	v_mul_f32_e32 v157, 0xbfb8aa3b, v157
	v_mul_f32_e32 v158, 0xbfb8aa3b, v158
	v_mul_f32_e32 v159, 0xbfb8aa3b, v159
	v_exp_f32_e32 v156, v156
	v_exp_f32_e32 v157, v157
	v_exp_f32_e32 v158, v158
	v_exp_f32_e32 v159, v159
	v_pk_add_f32 v[156:157], v[156:157], 1.0 op_sel_hi:[1,0]
	v_pk_add_f32 v[158:159], v[158:159], 1.0 op_sel_hi:[1,0]
	v_rcp_f32_e32 v156, v156
	v_rcp_f32_e32 v157, v157
	v_pk_mul_f32 v[158:159], v[158:159], s[78:79] op_sel_hi:[1,0]
	v_pk_mul_f32 v[158:159], v[156:157], v[158:159]
	v_pk_mul_f32 v[66:67], v[66:67], v[158:159]
	v_cvt_pk_f32_fp8_sdwa v[160:161], v194 src0_sel:WORD_1
	v_cvt_pk_f32_fp8_sdwa v[162:163], v196 src0_sel:WORD_1
	v_fmamk_f32 v160, v160, 0x3d800000, v8
	v_fmamk_f32 v161, v161, 0x3d800000, v9
	v_fmamk_f32 v162, v162, 0x3d800000, v16
	v_fmamk_f32 v163, v163, 0x3d800000, v17
	v_mul_f32_e32 v160, 0xbfb8aa3b, v160
	v_mul_f32_e32 v161, 0xbfb8aa3b, v161
	v_mul_f32_e32 v162, 0xbfb8aa3b, v162
	v_mul_f32_e32 v163, 0xbfb8aa3b, v163
	v_exp_f32_e32 v160, v160
	v_exp_f32_e32 v161, v161
	v_exp_f32_e32 v162, v162
	v_exp_f32_e32 v163, v163
	v_pk_add_f32 v[160:161], v[160:161], 1.0 op_sel_hi:[1,0]
	v_pk_add_f32 v[162:163], v[162:163], 1.0 op_sel_hi:[1,0]
	v_rcp_f32_e32 v160, v160
	v_rcp_f32_e32 v161, v161
	v_pk_mul_f32 v[162:163], v[162:163], s[78:79] op_sel_hi:[1,0]
	v_pk_mul_f32 v[162:163], v[160:161], v[162:163]
	v_pk_mul_f32 v[68:69], v[68:69], v[162:163]
	v_cvt_pk_f32_fp8_e32 v[156:157], v195
	v_cvt_pk_f32_fp8_e32 v[158:159], v197
	v_fmamk_f32 v156, v156, 0x3d800000, v10
	v_fmamk_f32 v157, v157, 0x3d800000, v11
	v_fmamk_f32 v158, v158, 0x3d800000, v18
	v_fmamk_f32 v159, v159, 0x3d800000, v19
	v_mul_f32_e32 v156, 0xbfb8aa3b, v156
	v_mul_f32_e32 v157, 0xbfb8aa3b, v157
	v_mul_f32_e32 v158, 0xbfb8aa3b, v158
	v_mul_f32_e32 v159, 0xbfb8aa3b, v159
	v_exp_f32_e32 v156, v156
	v_exp_f32_e32 v157, v157
	v_exp_f32_e32 v158, v158
	v_exp_f32_e32 v159, v159
	v_pk_add_f32 v[156:157], v[156:157], 1.0 op_sel_hi:[1,0]
	v_pk_add_f32 v[158:159], v[158:159], 1.0 op_sel_hi:[1,0]
	v_rcp_f32_e32 v156, v156
	v_rcp_f32_e32 v157, v157
	v_pk_mul_f32 v[158:159], v[158:159], s[78:79] op_sel_hi:[1,0]
	v_pk_mul_f32 v[158:159], v[156:157], v[158:159]
	v_pk_mul_f32 v[62:63], v[62:63], v[158:159]
	v_cvt_pk_f32_fp8_sdwa v[160:161], v195 src0_sel:WORD_1
	v_cvt_pk_f32_fp8_sdwa v[162:163], v197 src0_sel:WORD_1
	v_fmamk_f32 v160, v160, 0x3d800000, v12
	v_fmamk_f32 v161, v161, 0x3d800000, v13
	v_fmamk_f32 v162, v162, 0x3d800000, v20
	v_fmamk_f32 v163, v163, 0x3d800000, v21
	v_mul_f32_e32 v160, 0xbfb8aa3b, v160
	v_mul_f32_e32 v161, 0xbfb8aa3b, v161
	v_mul_f32_e32 v162, 0xbfb8aa3b, v162
	v_mul_f32_e32 v163, 0xbfb8aa3b, v163
	v_exp_f32_e32 v160, v160
	v_exp_f32_e32 v161, v161
	v_exp_f32_e32 v162, v162
	v_exp_f32_e32 v163, v163
	v_pk_add_f32 v[160:161], v[160:161], 1.0 op_sel_hi:[1,0]
	v_pk_add_f32 v[162:163], v[162:163], 1.0 op_sel_hi:[1,0]
	v_rcp_f32_e32 v160, v160
	v_rcp_f32_e32 v161, v161
	v_pk_mul_f32 v[162:163], v[162:163], s[78:79] op_sel_hi:[1,0]
	v_pk_mul_f32 v[162:163], v[160:161], v[162:163]
	v_pk_mul_f32 v[64:65], v[64:65], v[162:163]
	v_cvt_pk_f32_fp8_e32 v[156:157], v198
	v_cvt_pk_f32_fp8_e32 v[158:159], v218
	v_fmamk_f32 v156, v156, 0x3d800000, v6
	v_fmamk_f32 v157, v157, 0x3d800000, v7
	v_fmamk_f32 v158, v158, 0x3d800000, v14
	v_fmamk_f32 v159, v159, 0x3d800000, v15
	v_mul_f32_e32 v156, 0xbfb8aa3b, v156
	v_mul_f32_e32 v157, 0xbfb8aa3b, v157
	v_mul_f32_e32 v158, 0xbfb8aa3b, v158
	v_mul_f32_e32 v159, 0xbfb8aa3b, v159
	v_exp_f32_e32 v156, v156
	v_exp_f32_e32 v157, v157
	v_exp_f32_e32 v158, v158
	v_exp_f32_e32 v159, v159
	v_pk_add_f32 v[156:157], v[156:157], 1.0 op_sel_hi:[1,0]
	v_pk_add_f32 v[158:159], v[158:159], 1.0 op_sel_hi:[1,0]
	v_rcp_f32_e32 v156, v156
	v_rcp_f32_e32 v157, v157
	v_pk_mul_f32 v[158:159], v[158:159], s[78:79] op_sel_hi:[1,0]
	v_pk_mul_f32 v[158:159], v[156:157], v[158:159]
	v_pk_mul_f32 v[58:59], v[58:59], v[158:159]
	v_cvt_pk_f32_fp8_sdwa v[160:161], v198 src0_sel:WORD_1
	v_cvt_pk_f32_fp8_sdwa v[162:163], v218 src0_sel:WORD_1
	v_fmamk_f32 v160, v160, 0x3d800000, v8
	v_fmamk_f32 v161, v161, 0x3d800000, v9
	v_fmamk_f32 v162, v162, 0x3d800000, v16
	v_fmamk_f32 v163, v163, 0x3d800000, v17
	v_mul_f32_e32 v160, 0xbfb8aa3b, v160
	v_mul_f32_e32 v161, 0xbfb8aa3b, v161
	v_mul_f32_e32 v162, 0xbfb8aa3b, v162
	v_mul_f32_e32 v163, 0xbfb8aa3b, v163
	v_exp_f32_e32 v160, v160
	v_exp_f32_e32 v161, v161
	v_exp_f32_e32 v162, v162
	v_exp_f32_e32 v163, v163
	v_pk_add_f32 v[160:161], v[160:161], 1.0 op_sel_hi:[1,0]
	v_pk_add_f32 v[162:163], v[162:163], 1.0 op_sel_hi:[1,0]
	v_rcp_f32_e32 v160, v160
	v_rcp_f32_e32 v161, v161
	v_pk_mul_f32 v[162:163], v[162:163], s[78:79] op_sel_hi:[1,0]
	v_pk_mul_f32 v[162:163], v[160:161], v[162:163]
	v_pk_mul_f32 v[60:61], v[60:61], v[162:163]
	v_cvt_pk_f32_fp8_e32 v[156:157], v199
	v_cvt_pk_f32_fp8_e32 v[158:159], v219
	v_fmamk_f32 v156, v156, 0x3d800000, v10
	v_fmamk_f32 v157, v157, 0x3d800000, v11
	v_fmamk_f32 v158, v158, 0x3d800000, v18
	v_fmamk_f32 v159, v159, 0x3d800000, v19
	v_mul_f32_e32 v156, 0xbfb8aa3b, v156
	v_mul_f32_e32 v157, 0xbfb8aa3b, v157
	v_mul_f32_e32 v158, 0xbfb8aa3b, v158
	v_mul_f32_e32 v159, 0xbfb8aa3b, v159
	v_exp_f32_e32 v156, v156
	v_exp_f32_e32 v157, v157
	v_exp_f32_e32 v158, v158
	v_exp_f32_e32 v159, v159
	v_pk_add_f32 v[156:157], v[156:157], 1.0 op_sel_hi:[1,0]
	v_pk_add_f32 v[158:159], v[158:159], 1.0 op_sel_hi:[1,0]
	v_rcp_f32_e32 v156, v156
	v_rcp_f32_e32 v157, v157
	v_pk_mul_f32 v[158:159], v[158:159], s[78:79] op_sel_hi:[1,0]
	v_pk_mul_f32 v[158:159], v[156:157], v[158:159]
	v_pk_mul_f32 v[54:55], v[54:55], v[158:159]
	v_cvt_pk_f32_fp8_sdwa v[160:161], v199 src0_sel:WORD_1
	v_cvt_pk_f32_fp8_sdwa v[162:163], v219 src0_sel:WORD_1
	v_fmamk_f32 v160, v160, 0x3d800000, v12
	v_fmamk_f32 v161, v161, 0x3d800000, v13
	v_fmamk_f32 v162, v162, 0x3d800000, v20
	v_fmamk_f32 v163, v163, 0x3d800000, v21
	v_mul_f32_e32 v160, 0xbfb8aa3b, v160
	v_mul_f32_e32 v161, 0xbfb8aa3b, v161
	v_mul_f32_e32 v162, 0xbfb8aa3b, v162
	v_mul_f32_e32 v163, 0xbfb8aa3b, v163
	v_exp_f32_e32 v160, v160
	v_exp_f32_e32 v161, v161
	v_exp_f32_e32 v162, v162
	v_exp_f32_e32 v163, v163
	v_pk_add_f32 v[160:161], v[160:161], 1.0 op_sel_hi:[1,0]
	v_pk_add_f32 v[162:163], v[162:163], 1.0 op_sel_hi:[1,0]
	v_rcp_f32_e32 v160, v160
	v_rcp_f32_e32 v161, v161
	v_pk_mul_f32 v[162:163], v[162:163], s[78:79] op_sel_hi:[1,0]
	v_pk_mul_f32 v[162:163], v[160:161], v[162:163]
	v_pk_mul_f32 v[56:57], v[56:57], v[162:163]
	s_waitcnt vmcnt(4)
	v_cvt_pk_f32_fp8_e32 v[156:157], v178
	v_cvt_pk_f32_fp8_e32 v[158:159], v180
	v_fmamk_f32 v156, v156, 0x3d800000, v6
	v_fmamk_f32 v157, v157, 0x3d800000, v7
	v_fmamk_f32 v158, v158, 0x3d800000, v14
	v_fmamk_f32 v159, v159, 0x3d800000, v15
	v_mul_f32_e32 v156, 0xbfb8aa3b, v156
	v_mul_f32_e32 v157, 0xbfb8aa3b, v157
	v_mul_f32_e32 v158, 0xbfb8aa3b, v158
	v_mul_f32_e32 v159, 0xbfb8aa3b, v159
	v_exp_f32_e32 v156, v156
	v_exp_f32_e32 v157, v157
	v_exp_f32_e32 v158, v158
	v_exp_f32_e32 v159, v159
	v_pk_add_f32 v[156:157], v[156:157], 1.0 op_sel_hi:[1,0]
	v_pk_add_f32 v[158:159], v[158:159], 1.0 op_sel_hi:[1,0]
	v_rcp_f32_e32 v156, v156
	v_rcp_f32_e32 v157, v157
	v_pk_mul_f32 v[158:159], v[158:159], s[78:79] op_sel_hi:[1,0]
	v_pk_mul_f32 v[158:159], v[156:157], v[158:159]
	v_pk_mul_f32 v[50:51], v[50:51], v[158:159]
	v_cvt_pk_f32_fp8_sdwa v[160:161], v178 src0_sel:WORD_1
	v_cvt_pk_f32_fp8_sdwa v[162:163], v180 src0_sel:WORD_1
	v_fmamk_f32 v160, v160, 0x3d800000, v8
	v_fmamk_f32 v161, v161, 0x3d800000, v9
	v_fmamk_f32 v162, v162, 0x3d800000, v16
	v_fmamk_f32 v163, v163, 0x3d800000, v17
	v_mul_f32_e32 v160, 0xbfb8aa3b, v160
	v_mul_f32_e32 v161, 0xbfb8aa3b, v161
	v_mul_f32_e32 v162, 0xbfb8aa3b, v162
	v_mul_f32_e32 v163, 0xbfb8aa3b, v163
	v_exp_f32_e32 v160, v160
	v_exp_f32_e32 v161, v161
	v_exp_f32_e32 v162, v162
	v_exp_f32_e32 v163, v163
	v_pk_add_f32 v[160:161], v[160:161], 1.0 op_sel_hi:[1,0]
	v_pk_add_f32 v[162:163], v[162:163], 1.0 op_sel_hi:[1,0]
	v_rcp_f32_e32 v160, v160
	v_rcp_f32_e32 v161, v161
	v_pk_mul_f32 v[162:163], v[162:163], s[78:79] op_sel_hi:[1,0]
	v_pk_mul_f32 v[162:163], v[160:161], v[162:163]
	v_pk_mul_f32 v[52:53], v[52:53], v[162:163]
	v_cvt_pk_f32_fp8_e32 v[156:157], v179
	v_cvt_pk_f32_fp8_e32 v[158:159], v181
	v_fmamk_f32 v156, v156, 0x3d800000, v10
	v_fmamk_f32 v157, v157, 0x3d800000, v11
	v_fmamk_f32 v158, v158, 0x3d800000, v18
	v_fmamk_f32 v159, v159, 0x3d800000, v19
	v_mul_f32_e32 v156, 0xbfb8aa3b, v156
	v_mul_f32_e32 v157, 0xbfb8aa3b, v157
	v_mul_f32_e32 v158, 0xbfb8aa3b, v158
	v_mul_f32_e32 v159, 0xbfb8aa3b, v159
	v_exp_f32_e32 v156, v156
	v_exp_f32_e32 v157, v157
	v_exp_f32_e32 v158, v158
	v_exp_f32_e32 v159, v159
	v_pk_add_f32 v[156:157], v[156:157], 1.0 op_sel_hi:[1,0]
	v_pk_add_f32 v[158:159], v[158:159], 1.0 op_sel_hi:[1,0]
	v_rcp_f32_e32 v156, v156
	v_rcp_f32_e32 v157, v157
	v_pk_mul_f32 v[158:159], v[158:159], s[78:79] op_sel_hi:[1,0]
	v_pk_mul_f32 v[158:159], v[156:157], v[158:159]
	v_pk_mul_f32 v[46:47], v[46:47], v[158:159]
	v_cvt_pk_f32_fp8_sdwa v[160:161], v179 src0_sel:WORD_1
	v_cvt_pk_f32_fp8_sdwa v[162:163], v181 src0_sel:WORD_1
	v_fmamk_f32 v160, v160, 0x3d800000, v12
	v_fmamk_f32 v161, v161, 0x3d800000, v13
	v_fmamk_f32 v162, v162, 0x3d800000, v20
	v_fmamk_f32 v163, v163, 0x3d800000, v21
	v_mul_f32_e32 v160, 0xbfb8aa3b, v160
	v_mul_f32_e32 v161, 0xbfb8aa3b, v161
	v_mul_f32_e32 v162, 0xbfb8aa3b, v162
	v_mul_f32_e32 v163, 0xbfb8aa3b, v163
	v_exp_f32_e32 v160, v160
	v_exp_f32_e32 v161, v161
	v_exp_f32_e32 v162, v162
	v_exp_f32_e32 v163, v163
	v_pk_add_f32 v[160:161], v[160:161], 1.0 op_sel_hi:[1,0]
	v_pk_add_f32 v[162:163], v[162:163], 1.0 op_sel_hi:[1,0]
	v_rcp_f32_e32 v160, v160
	v_rcp_f32_e32 v161, v161
	v_pk_mul_f32 v[162:163], v[162:163], s[78:79] op_sel_hi:[1,0]
	v_pk_mul_f32 v[162:163], v[160:161], v[162:163]
	v_pk_mul_f32 v[48:49], v[48:49], v[162:163]
	v_cvt_pk_f32_fp8_e32 v[156:157], v182
	v_cvt_pk_f32_fp8_e32 v[158:159], v184
	v_fmamk_f32 v156, v156, 0x3d800000, v6
	v_fmamk_f32 v157, v157, 0x3d800000, v7
	v_fmamk_f32 v158, v158, 0x3d800000, v14
	v_fmamk_f32 v159, v159, 0x3d800000, v15
	v_mul_f32_e32 v156, 0xbfb8aa3b, v156
	v_mul_f32_e32 v157, 0xbfb8aa3b, v157
	v_mul_f32_e32 v158, 0xbfb8aa3b, v158
	v_mul_f32_e32 v159, 0xbfb8aa3b, v159
	v_exp_f32_e32 v156, v156
	v_exp_f32_e32 v157, v157
	v_exp_f32_e32 v158, v158
	v_exp_f32_e32 v159, v159
	v_pk_add_f32 v[156:157], v[156:157], 1.0 op_sel_hi:[1,0]
	v_pk_add_f32 v[158:159], v[158:159], 1.0 op_sel_hi:[1,0]
	v_rcp_f32_e32 v156, v156
	v_rcp_f32_e32 v157, v157
	v_pk_mul_f32 v[158:159], v[158:159], s[78:79] op_sel_hi:[1,0]
	v_pk_mul_f32 v[158:159], v[156:157], v[158:159]
	v_pk_mul_f32 v[42:43], v[42:43], v[158:159]
	v_cvt_pk_f32_fp8_sdwa v[160:161], v182 src0_sel:WORD_1
	v_cvt_pk_f32_fp8_sdwa v[162:163], v184 src0_sel:WORD_1
	v_fmamk_f32 v160, v160, 0x3d800000, v8
	v_fmamk_f32 v161, v161, 0x3d800000, v9
	v_fmamk_f32 v162, v162, 0x3d800000, v16
	v_fmamk_f32 v163, v163, 0x3d800000, v17
	v_mul_f32_e32 v160, 0xbfb8aa3b, v160
	v_mul_f32_e32 v161, 0xbfb8aa3b, v161
	v_mul_f32_e32 v162, 0xbfb8aa3b, v162
	v_mul_f32_e32 v163, 0xbfb8aa3b, v163
	v_exp_f32_e32 v160, v160
	v_exp_f32_e32 v161, v161
	v_exp_f32_e32 v162, v162
	v_exp_f32_e32 v163, v163
	v_pk_add_f32 v[160:161], v[160:161], 1.0 op_sel_hi:[1,0]
	v_pk_add_f32 v[162:163], v[162:163], 1.0 op_sel_hi:[1,0]
	v_rcp_f32_e32 v160, v160
	v_rcp_f32_e32 v161, v161
	v_pk_mul_f32 v[162:163], v[162:163], s[78:79] op_sel_hi:[1,0]
	v_pk_mul_f32 v[162:163], v[160:161], v[162:163]
	v_pk_mul_f32 v[44:45], v[44:45], v[162:163]
	v_cvt_pk_f32_fp8_e32 v[156:157], v183
	v_cvt_pk_f32_fp8_e32 v[158:159], v185
	v_fmamk_f32 v156, v156, 0x3d800000, v10
	v_fmamk_f32 v157, v157, 0x3d800000, v11
	v_fmamk_f32 v158, v158, 0x3d800000, v18
	v_fmamk_f32 v159, v159, 0x3d800000, v19
	v_mul_f32_e32 v156, 0xbfb8aa3b, v156
	v_mul_f32_e32 v157, 0xbfb8aa3b, v157
	v_mul_f32_e32 v158, 0xbfb8aa3b, v158
	v_mul_f32_e32 v159, 0xbfb8aa3b, v159
	v_exp_f32_e32 v156, v156
	v_exp_f32_e32 v157, v157
	v_exp_f32_e32 v158, v158
	v_exp_f32_e32 v159, v159
	v_pk_add_f32 v[156:157], v[156:157], 1.0 op_sel_hi:[1,0]
	v_pk_add_f32 v[158:159], v[158:159], 1.0 op_sel_hi:[1,0]
	v_rcp_f32_e32 v156, v156
	v_rcp_f32_e32 v157, v157
	v_pk_mul_f32 v[158:159], v[158:159], s[78:79] op_sel_hi:[1,0]
	v_pk_mul_f32 v[158:159], v[156:157], v[158:159]
	v_pk_mul_f32 v[38:39], v[38:39], v[158:159]
	v_cvt_pk_f32_fp8_sdwa v[160:161], v183 src0_sel:WORD_1
	v_cvt_pk_f32_fp8_sdwa v[162:163], v185 src0_sel:WORD_1
	v_fmamk_f32 v160, v160, 0x3d800000, v12
	v_fmamk_f32 v161, v161, 0x3d800000, v13
	v_fmamk_f32 v162, v162, 0x3d800000, v20
	v_fmamk_f32 v163, v163, 0x3d800000, v21
	v_mul_f32_e32 v160, 0xbfb8aa3b, v160
	v_mul_f32_e32 v161, 0xbfb8aa3b, v161
	v_mul_f32_e32 v162, 0xbfb8aa3b, v162
	v_mul_f32_e32 v163, 0xbfb8aa3b, v163
	v_exp_f32_e32 v160, v160
	v_exp_f32_e32 v161, v161
	v_exp_f32_e32 v162, v162
	v_exp_f32_e32 v163, v163
	v_pk_add_f32 v[160:161], v[160:161], 1.0 op_sel_hi:[1,0]
	v_pk_add_f32 v[162:163], v[162:163], 1.0 op_sel_hi:[1,0]
	v_rcp_f32_e32 v160, v160
	v_rcp_f32_e32 v161, v161
	v_pk_mul_f32 v[162:163], v[162:163], s[78:79] op_sel_hi:[1,0]
	v_pk_mul_f32 v[162:163], v[160:161], v[162:163]
	v_pk_mul_f32 v[40:41], v[40:41], v[162:163]
	s_waitcnt vmcnt(0)
	v_cvt_pk_f32_fp8_e32 v[156:157], v186
	v_cvt_pk_f32_fp8_e32 v[158:159], v188
	v_fmamk_f32 v156, v156, 0x3d800000, v6
	v_fmamk_f32 v157, v157, 0x3d800000, v7
	v_fmamk_f32 v158, v158, 0x3d800000, v14
	v_fmamk_f32 v159, v159, 0x3d800000, v15
	v_mul_f32_e32 v156, 0xbfb8aa3b, v156
	v_mul_f32_e32 v157, 0xbfb8aa3b, v157
	v_mul_f32_e32 v158, 0xbfb8aa3b, v158
	v_mul_f32_e32 v159, 0xbfb8aa3b, v159
	v_exp_f32_e32 v156, v156
	v_exp_f32_e32 v157, v157
	v_exp_f32_e32 v158, v158
	v_exp_f32_e32 v159, v159
	v_pk_add_f32 v[156:157], v[156:157], 1.0 op_sel_hi:[1,0]
	v_pk_add_f32 v[158:159], v[158:159], 1.0 op_sel_hi:[1,0]
	v_rcp_f32_e32 v156, v156
	v_rcp_f32_e32 v157, v157
	v_pk_mul_f32 v[158:159], v[158:159], s[78:79] op_sel_hi:[1,0]
	v_pk_mul_f32 v[158:159], v[156:157], v[158:159]
	v_pk_mul_f32 v[34:35], v[34:35], v[158:159]
	v_cvt_pk_f32_fp8_sdwa v[160:161], v186 src0_sel:WORD_1
	v_cvt_pk_f32_fp8_sdwa v[162:163], v188 src0_sel:WORD_1
	v_fmamk_f32 v160, v160, 0x3d800000, v8
	v_fmamk_f32 v161, v161, 0x3d800000, v9
	v_fmamk_f32 v162, v162, 0x3d800000, v16
	v_fmamk_f32 v163, v163, 0x3d800000, v17
	v_mul_f32_e32 v160, 0xbfb8aa3b, v160
	v_mul_f32_e32 v161, 0xbfb8aa3b, v161
	v_mul_f32_e32 v162, 0xbfb8aa3b, v162
	v_mul_f32_e32 v163, 0xbfb8aa3b, v163
	v_exp_f32_e32 v160, v160
	v_exp_f32_e32 v161, v161
	v_exp_f32_e32 v162, v162
	v_exp_f32_e32 v163, v163
	v_pk_add_f32 v[160:161], v[160:161], 1.0 op_sel_hi:[1,0]
	v_pk_add_f32 v[162:163], v[162:163], 1.0 op_sel_hi:[1,0]
	v_rcp_f32_e32 v160, v160
	v_rcp_f32_e32 v161, v161
	v_pk_mul_f32 v[162:163], v[162:163], s[78:79] op_sel_hi:[1,0]
	v_pk_mul_f32 v[162:163], v[160:161], v[162:163]
	v_pk_mul_f32 v[36:37], v[36:37], v[162:163]
	v_cvt_pk_f32_fp8_e32 v[156:157], v187
	v_cvt_pk_f32_fp8_e32 v[158:159], v189
	v_fmamk_f32 v156, v156, 0x3d800000, v10
	v_fmamk_f32 v157, v157, 0x3d800000, v11
	v_fmamk_f32 v158, v158, 0x3d800000, v18
	v_fmamk_f32 v159, v159, 0x3d800000, v19
	v_mul_f32_e32 v156, 0xbfb8aa3b, v156
	v_mul_f32_e32 v157, 0xbfb8aa3b, v157
	v_mul_f32_e32 v158, 0xbfb8aa3b, v158
	v_mul_f32_e32 v159, 0xbfb8aa3b, v159
	v_exp_f32_e32 v156, v156
	v_exp_f32_e32 v157, v157
	v_exp_f32_e32 v158, v158
	v_exp_f32_e32 v159, v159
	v_pk_add_f32 v[156:157], v[156:157], 1.0 op_sel_hi:[1,0]
	v_pk_add_f32 v[158:159], v[158:159], 1.0 op_sel_hi:[1,0]
	v_rcp_f32_e32 v156, v156
	v_rcp_f32_e32 v157, v157
	v_pk_mul_f32 v[158:159], v[158:159], s[78:79] op_sel_hi:[1,0]
	v_pk_mul_f32 v[158:159], v[156:157], v[158:159]
	v_pk_mul_f32 v[30:31], v[30:31], v[158:159]
	v_cvt_pk_f32_fp8_sdwa v[160:161], v187 src0_sel:WORD_1
	v_cvt_pk_f32_fp8_sdwa v[162:163], v189 src0_sel:WORD_1
	v_fmamk_f32 v160, v160, 0x3d800000, v12
	v_fmamk_f32 v161, v161, 0x3d800000, v13
	v_fmamk_f32 v162, v162, 0x3d800000, v20
	v_fmamk_f32 v163, v163, 0x3d800000, v21
	v_mul_f32_e32 v160, 0xbfb8aa3b, v160
	v_mul_f32_e32 v161, 0xbfb8aa3b, v161
	v_mul_f32_e32 v162, 0xbfb8aa3b, v162
	v_mul_f32_e32 v163, 0xbfb8aa3b, v163
	v_exp_f32_e32 v160, v160
	v_exp_f32_e32 v161, v161
	v_exp_f32_e32 v162, v162
	v_exp_f32_e32 v163, v163
	v_pk_add_f32 v[160:161], v[160:161], 1.0 op_sel_hi:[1,0]
	v_pk_add_f32 v[162:163], v[162:163], 1.0 op_sel_hi:[1,0]
	v_rcp_f32_e32 v160, v160
	v_rcp_f32_e32 v161, v161
	v_pk_mul_f32 v[162:163], v[162:163], s[78:79] op_sel_hi:[1,0]
	v_pk_mul_f32 v[162:163], v[160:161], v[162:163]
	v_pk_mul_f32 v[32:33], v[32:33], v[162:163]
	v_cvt_pk_f32_fp8_e32 v[156:157], v190
	v_cvt_pk_f32_fp8_e32 v[158:159], v192
	v_fmamk_f32 v156, v156, 0x3d800000, v6
	v_fmamk_f32 v157, v157, 0x3d800000, v7
	v_fmamk_f32 v158, v158, 0x3d800000, v14
	v_fmamk_f32 v159, v159, 0x3d800000, v15
	v_mul_f32_e32 v156, 0xbfb8aa3b, v156
	v_mul_f32_e32 v157, 0xbfb8aa3b, v157
	v_mul_f32_e32 v158, 0xbfb8aa3b, v158
	v_mul_f32_e32 v159, 0xbfb8aa3b, v159
	v_exp_f32_e32 v156, v156
	v_exp_f32_e32 v157, v157
	v_exp_f32_e32 v158, v158
	v_exp_f32_e32 v159, v159
	v_pk_add_f32 v[156:157], v[156:157], 1.0 op_sel_hi:[1,0]
	v_pk_add_f32 v[158:159], v[158:159], 1.0 op_sel_hi:[1,0]
	v_rcp_f32_e32 v156, v156
	v_rcp_f32_e32 v157, v157
	v_pk_mul_f32 v[158:159], v[158:159], s[78:79] op_sel_hi:[1,0]
	v_pk_mul_f32 v[158:159], v[156:157], v[158:159]
	v_pk_mul_f32 v[26:27], v[26:27], v[158:159]
	v_cvt_pk_f32_fp8_sdwa v[160:161], v190 src0_sel:WORD_1
	v_cvt_pk_f32_fp8_sdwa v[162:163], v192 src0_sel:WORD_1
	v_fmamk_f32 v160, v160, 0x3d800000, v8
	v_fmamk_f32 v161, v161, 0x3d800000, v9
	v_fmamk_f32 v162, v162, 0x3d800000, v16
	v_fmamk_f32 v163, v163, 0x3d800000, v17
	v_mul_f32_e32 v160, 0xbfb8aa3b, v160
	v_mul_f32_e32 v161, 0xbfb8aa3b, v161
	v_mul_f32_e32 v162, 0xbfb8aa3b, v162
	v_mul_f32_e32 v163, 0xbfb8aa3b, v163
	v_exp_f32_e32 v160, v160
	v_exp_f32_e32 v161, v161
	v_exp_f32_e32 v162, v162
	v_exp_f32_e32 v163, v163
	v_pk_add_f32 v[160:161], v[160:161], 1.0 op_sel_hi:[1,0]
	v_pk_add_f32 v[162:163], v[162:163], 1.0 op_sel_hi:[1,0]
	v_rcp_f32_e32 v160, v160
	v_rcp_f32_e32 v161, v161
	v_pk_mul_f32 v[162:163], v[162:163], s[78:79] op_sel_hi:[1,0]
	v_pk_mul_f32 v[162:163], v[160:161], v[162:163]
	v_pk_mul_f32 v[28:29], v[28:29], v[162:163]
	v_cvt_pk_f32_fp8_e32 v[156:157], v191
	v_cvt_pk_f32_fp8_e32 v[158:159], v193
	v_fmamk_f32 v156, v156, 0x3d800000, v10
	v_fmamk_f32 v157, v157, 0x3d800000, v11
	v_fmamk_f32 v158, v158, 0x3d800000, v18
	v_fmamk_f32 v159, v159, 0x3d800000, v19
	v_mul_f32_e32 v156, 0xbfb8aa3b, v156
	v_mul_f32_e32 v157, 0xbfb8aa3b, v157
	v_mul_f32_e32 v158, 0xbfb8aa3b, v158
	v_mul_f32_e32 v159, 0xbfb8aa3b, v159
	v_exp_f32_e32 v156, v156
	v_exp_f32_e32 v157, v157
	v_exp_f32_e32 v158, v158
	v_exp_f32_e32 v159, v159
	v_pk_add_f32 v[156:157], v[156:157], 1.0 op_sel_hi:[1,0]
	v_pk_add_f32 v[158:159], v[158:159], 1.0 op_sel_hi:[1,0]
	v_rcp_f32_e32 v156, v156
	v_rcp_f32_e32 v157, v157
	v_pk_mul_f32 v[158:159], v[158:159], s[78:79] op_sel_hi:[1,0]
	v_pk_mul_f32 v[158:159], v[156:157], v[158:159]
	v_pk_mul_f32 v[22:23], v[22:23], v[158:159]
	v_cvt_pk_f32_fp8_sdwa v[160:161], v191 src0_sel:WORD_1
	v_cvt_pk_f32_fp8_sdwa v[162:163], v193 src0_sel:WORD_1
	v_fmamk_f32 v160, v160, 0x3d800000, v12
	v_fmamk_f32 v161, v161, 0x3d800000, v13
	v_fmamk_f32 v162, v162, 0x3d800000, v20
	v_fmamk_f32 v163, v163, 0x3d800000, v21
	v_mul_f32_e32 v160, 0xbfb8aa3b, v160
	v_mul_f32_e32 v161, 0xbfb8aa3b, v161
	v_mul_f32_e32 v162, 0xbfb8aa3b, v162
	v_mul_f32_e32 v163, 0xbfb8aa3b, v163
	v_exp_f32_e32 v160, v160
	v_exp_f32_e32 v161, v161
	v_exp_f32_e32 v162, v162
	v_exp_f32_e32 v163, v163
	v_pk_add_f32 v[160:161], v[160:161], 1.0 op_sel_hi:[1,0]
	v_pk_add_f32 v[162:163], v[162:163], 1.0 op_sel_hi:[1,0]
	v_rcp_f32_e32 v160, v160
	v_rcp_f32_e32 v161, v161
	v_pk_mul_f32 v[162:163], v[162:163], s[78:79] op_sel_hi:[1,0]
	v_pk_mul_f32 v[162:163], v[160:161], v[162:163]
	v_pk_mul_f32 v[24:25], v[24:25], v[162:163]
	s_mov_b64 s[50:51], 0x1a0080
